# P10 cooperative prefetch: B-slab slice rank taken from the workgroup's real index (s33 = bid>>3) instead of a stale register
# speedup vs baseline: 1.0140x; 1.0107x over previous
.LBB0_1441:
	s_and_b64 vcc, exec, s[0:1]
	s_cmp_eq_u32 s98, 0
	s_cbranch_scc1 .Lgk_first_p10
	v_mov_b32_e32 v175, v169
	v_mov_b32_e32 v173, v169
	s_mov_b32 s23, 0
	s_mov_b64 s[34:35], 0x100
	s_mov_b64 s[36:37], s[16:17]
	v_readfirstlane_b32 s70, v0
	s_lshr_b32 s70, s70, 6
	s_cmp_eq_u64 s[2:3], 0
	s_cselect_b32 s71, s65, s66
	s_lshl_b32 s71, s71, 17
	s_lshl_b32 s72, s28, 14
	s_add_u32 s71, s71, s72
	s_and_b32 s72, s70, 1
	s_lshl_b32 s72, s72, 13
	s_add_u32 s71, s71, s72
	s_add_u32 s74, s12, s71
	s_addc_u32 s75, s13, 0
	s_bfe_u32 s72, s33, 0x20003
	s_lshl_b32 s72, s72, 15
	s_sub_u32 s73, s70, 2
	s_lshl_b32 s78, s73, 13
	s_add_u32 s72, s72, s78
	s_add_u32 s76, s26, s72
	s_addc_u32 s77, s27, 0
	s_cmp_lt_u32 s73, 4
	s_cselect_b64 s[74:75], s[76:77], s[74:75]
	v_lshlrev_b32_e32 v250, 7, v206
	ds_read_b128 v[26:29], v191
	ds_read_b128 v[30:33], v191 offset:1024
	ds_read_b128 v[18:21], v191 offset:2048
	ds_read_b128 v[22:25], v191 offset:3072
	ds_read_b128 v[10:13], v192
	ds_read_b128 v[14:17], v192 offset:1024
	ds_read_b128 v[2:5], v192 offset:2048
	ds_read_b128 v[6:9], v192 offset:3072
	s_cmp_eq_u32 s54, s23
	s_cselect_b64 vcc, -1, 0
	s_add_i32 s23, s23, 2
	s_and_b64 s[38:39], vcc, exec
	s_cselect_b32 s38, 0, s34
	s_cselect_b32 s25, 0, s35
	s_add_u32 s38, s12, s38
	s_addc_u32 s39, s13, s25
	s_add_u32 s25, s30, s34
	s_addc_u32 s67, s31, s35
	s_and_b64 s[40:41], vcc, exec
	v_cndmask_b32_e32 v168, v197, v198, vcc
	v_cndmask_b32_e32 v202, v172, v200, vcc
	v_cndmask_b32_e32 v184, v170, v199, vcc
	s_cselect_b32 s41, s27, s67
	s_cselect_b32 s40, s26, s25
	s_mov_b32 m0, s55
	v_lshl_add_u64 v[186:187], s[36:37], 0, v[172:173]
	ds_read_b128 v[176:179], v193
	ds_read_b128 v[180:183], v193 offset:1024
	ds_read_b128 v[208:211], v193 offset:2048
	ds_read_b128 v[212:215], v193 offset:3072
	ds_read_b128 v[216:219], v193 offset:4096
	ds_read_b128 v[220:223], v193 offset:5120
	ds_read_b128 v[224:227], v193 offset:6144
	ds_read_b128 v[228:231], v193 offset:7168
	global_load_lds_dwordx4 v[186:187], off
	v_lshl_add_u64 v[186:187], s[36:37], 0, v[174:175]
	s_mov_b32 m0, s56
	s_nop 0
	global_load_lds_dwordx4 v[186:187], off
	s_waitcnt vmcnt(16)
	s_waitcnt lgkmcnt(0)
	s_barrier
	s_setprio 1
	s_waitcnt lgkmcnt(0)
	v_mfma_scale_f32_16x16x128_f8f6f4 v[158:161], v[26:33], v[176:183], 0, v188, v189 op_sel_hi:[0,0,0]
	v_mfma_scale_f32_16x16x128_f8f6f4 v[154:157], v[18:25], v[176:183], 0, v188, v189 op_sel_hi:[0,0,0]
	v_mfma_scale_f32_16x16x128_f8f6f4 v[142:145], v[26:33], v[208:215], 0, v188, v189 op_sel_hi:[0,0,0]
	v_mfma_scale_f32_16x16x128_f8f6f4 v[138:141], v[18:25], v[208:215], 0, v188, v189 op_sel_hi:[0,0,0]
	v_mfma_scale_f32_16x16x128_f8f6f4 v[126:129], v[26:33], v[216:223], 0, v188, v189 op_sel_hi:[0,0,0]
	v_mfma_scale_f32_16x16x128_f8f6f4 v[122:125], v[18:25], v[216:223], 0, v188, v189 op_sel_hi:[0,0,0]
	v_mfma_scale_f32_16x16x128_f8f6f4 v[110:113], v[26:33], v[224:231], 0, v188, v189 op_sel_hi:[0,0,0]
	v_mfma_scale_f32_16x16x128_f8f6f4 v[106:109], v[18:25], v[224:231], 0, v188, v189 op_sel_hi:[0,0,0]
	s_setprio 0
	s_setprio 1
	v_mfma_scale_f32_16x16x128_f8f6f4 v[150:153], v[10:17], v[176:183], 0, v188, v189 op_sel_hi:[0,0,0]
	v_mfma_scale_f32_16x16x128_f8f6f4 v[146:149], v[2:9], v[176:183], 0, v188, v189 op_sel_hi:[0,0,0]
	v_mfma_scale_f32_16x16x128_f8f6f4 v[134:137], v[10:17], v[208:215], 0, v188, v189 op_sel_hi:[0,0,0]
	v_mfma_scale_f32_16x16x128_f8f6f4 v[130:133], v[2:9], v[208:215], 0, v188, v189 op_sel_hi:[0,0,0]
	v_mfma_scale_f32_16x16x128_f8f6f4 v[118:121], v[10:17], v[216:223], 0, v188, v189 op_sel_hi:[0,0,0]
	v_mfma_scale_f32_16x16x128_f8f6f4 v[114:117], v[2:9], v[216:223], 0, v188, v189 op_sel_hi:[0,0,0]
	v_mfma_scale_f32_16x16x128_f8f6f4 v[102:105], v[10:17], v[224:231], 0, v188, v189 op_sel_hi:[0,0,0]
	v_mfma_scale_f32_16x16x128_f8f6f4 v[98:101], v[2:9], v[224:231], 0, v188, v189 op_sel_hi:[0,0,0]
	s_setprio 0
	s_barrier
	s_mov_b32 m0, s57
	v_lshl_add_u64 v[176:177], s[40:41], 0, v[166:167]
	v_lshl_add_u64 v[178:179], s[40:41], 0, v[164:165]
	s_add_u32 s40, s40, s10
	ds_read_b128 v[208:211], v193 offset:16384
	ds_read_b128 v[212:215], v193 offset:17408
	ds_read_b128 v[216:219], v193 offset:18432
	ds_read_b128 v[220:223], v193 offset:19456
	ds_read_b128 v[224:227], v193 offset:20480
	ds_read_b128 v[228:231], v193 offset:21504
	ds_read_b128 v[232:235], v193 offset:22528
	ds_read_b128 v[236:239], v193 offset:23552
	global_load_lds_dwordx4 v[176:177], off
	s_mov_b32 m0, s58
	s_addc_u32 s41, s41, s11
	global_load_lds_dwordx4 v[178:179], off
	v_lshl_add_u64 v[180:181], s[40:41], 0, v[166:167]
	s_mov_b32 m0, s59
	v_lshl_add_u64 v[182:183], s[40:41], 0, v[164:165]
	global_load_lds_dwordx4 v[180:181], off
	s_mov_b32 m0, s60
	v_mov_b32_e32 v185, v169
	global_load_lds_dwordx4 v[182:183], off
	s_mov_b32 m0, s29
	v_lshl_add_u64 v[186:187], s[38:39], 0, v[168:169]
	global_load_lds_dwordx4 v168, s[38:39]
	s_mov_b32 m0, s46
	s_nop 0
	global_load_lds_dwordx4 v184, s[38:39]
	global_load_dword v251, v250, s[74:75]
	s_waitcnt vmcnt(17)
	s_waitcnt lgkmcnt(0)
	v_lshl_add_u64 v[184:185], s[38:39], 0, v[184:185]
	s_barrier
	s_setprio 1
	s_waitcnt lgkmcnt(0)
	v_mfma_scale_f32_16x16x128_f8f6f4 v[94:97], v[26:33], v[208:215], 0, v188, v189 op_sel_hi:[0,0,0]
	v_mfma_scale_f32_16x16x128_f8f6f4 v[90:93], v[18:25], v[208:215], 0, v188, v189 op_sel_hi:[0,0,0]
	v_mfma_scale_f32_16x16x128_f8f6f4 v[78:81], v[26:33], v[216:223], 0, v188, v189 op_sel_hi:[0,0,0]
	v_mfma_scale_f32_16x16x128_f8f6f4 v[74:77], v[18:25], v[216:223], 0, v188, v189 op_sel_hi:[0,0,0]
	v_mfma_scale_f32_16x16x128_f8f6f4 v[62:65], v[26:33], v[224:231], 0, v188, v189 op_sel_hi:[0,0,0]
	v_mfma_scale_f32_16x16x128_f8f6f4 v[58:61], v[18:25], v[224:231], 0, v188, v189 op_sel_hi:[0,0,0]
	v_mfma_scale_f32_16x16x128_f8f6f4 v[46:49], v[26:33], v[232:239], 0, v188, v189 op_sel_hi:[0,0,0]
	v_mfma_scale_f32_16x16x128_f8f6f4 v[42:45], v[18:25], v[232:239], 0, v188, v189 op_sel_hi:[0,0,0]
	s_setprio 0
	s_setprio 1
	v_mfma_scale_f32_16x16x128_f8f6f4 v[86:89], v[10:17], v[208:215], 0, v188, v189 op_sel_hi:[0,0,0]
	v_mfma_scale_f32_16x16x128_f8f6f4 v[82:85], v[2:9], v[208:215], 0, v188, v189 op_sel_hi:[0,0,0]
	v_mfma_scale_f32_16x16x128_f8f6f4 v[70:73], v[10:17], v[216:223], 0, v188, v189 op_sel_hi:[0,0,0]
	v_mfma_scale_f32_16x16x128_f8f6f4 v[66:69], v[2:9], v[216:223], 0, v188, v189 op_sel_hi:[0,0,0]
	v_mfma_scale_f32_16x16x128_f8f6f4 v[54:57], v[10:17], v[224:231], 0, v188, v189 op_sel_hi:[0,0,0]
	v_mfma_scale_f32_16x16x128_f8f6f4 v[50:53], v[2:9], v[224:231], 0, v188, v189 op_sel_hi:[0,0,0]
	v_mfma_scale_f32_16x16x128_f8f6f4 v[38:41], v[10:17], v[232:239], 0, v188, v189 op_sel_hi:[0,0,0]
	v_mfma_scale_f32_16x16x128_f8f6f4 v[34:37], v[2:9], v[232:239], 0, v188, v189 op_sel_hi:[0,0,0]
	s_setprio 0
	s_barrier
	ds_read_b128 v[26:29], v194
	ds_read_b128 v[30:33], v194 offset:1024
	ds_read_b128 v[18:21], v194 offset:2048
	ds_read_b128 v[22:25], v194 offset:3072
	ds_read_b128 v[10:13], v195
	ds_read_b128 v[14:17], v195 offset:1024
	ds_read_b128 v[2:5], v195 offset:2048
	ds_read_b128 v[6:9], v195 offset:3072
	s_mov_b32 m0, s47
	ds_read_b128 v[208:211], v193 offset:32768
	ds_read_b128 v[212:215], v193 offset:33792
	ds_read_b128 v[216:219], v193 offset:34816
	ds_read_b128 v[220:223], v193 offset:35840
	ds_read_b128 v[224:227], v193 offset:36864
	ds_read_b128 v[228:231], v193 offset:37888
	ds_read_b128 v[232:235], v193 offset:38912
	ds_read_b128 v[236:239], v193 offset:39936
	v_cndmask_b32_e32 v168, v174, v201, vcc
	global_load_lds_dwordx4 v202, s[38:39]
	s_mov_b32 m0, s48
	s_nop 0
	global_load_lds_dwordx4 v168, s[38:39]
	s_waitcnt vmcnt(9)
	s_waitcnt lgkmcnt(0)
	s_barrier
	s_setprio 1
	s_waitcnt lgkmcnt(0)
	v_mfma_scale_f32_16x16x128_f8f6f4 v[158:161], v[26:33], v[208:215], v[158:161], v188, v189 op_sel_hi:[0,0,0]
	v_mfma_scale_f32_16x16x128_f8f6f4 v[154:157], v[18:25], v[208:215], v[154:157], v188, v189 op_sel_hi:[0,0,0]
	v_mfma_scale_f32_16x16x128_f8f6f4 v[142:145], v[26:33], v[216:223], v[142:145], v188, v189 op_sel_hi:[0,0,0]
	v_mfma_scale_f32_16x16x128_f8f6f4 v[138:141], v[18:25], v[216:223], v[138:141], v188, v189 op_sel_hi:[0,0,0]
	v_mfma_scale_f32_16x16x128_f8f6f4 v[126:129], v[26:33], v[224:231], v[126:129], v188, v189 op_sel_hi:[0,0,0]
	v_mfma_scale_f32_16x16x128_f8f6f4 v[122:125], v[18:25], v[224:231], v[122:125], v188, v189 op_sel_hi:[0,0,0]
	v_mfma_scale_f32_16x16x128_f8f6f4 v[110:113], v[26:33], v[232:239], v[110:113], v188, v189 op_sel_hi:[0,0,0]
	v_mfma_scale_f32_16x16x128_f8f6f4 v[106:109], v[18:25], v[232:239], v[106:109], v188, v189 op_sel_hi:[0,0,0]
	s_setprio 0
	s_setprio 1
	v_mfma_scale_f32_16x16x128_f8f6f4 v[150:153], v[10:17], v[208:215], v[150:153], v188, v189 op_sel_hi:[0,0,0]
	v_mfma_scale_f32_16x16x128_f8f6f4 v[146:149], v[2:9], v[208:215], v[146:149], v188, v189 op_sel_hi:[0,0,0]
	v_mfma_scale_f32_16x16x128_f8f6f4 v[134:137], v[10:17], v[216:223], v[134:137], v188, v189 op_sel_hi:[0,0,0]
	v_mfma_scale_f32_16x16x128_f8f6f4 v[130:133], v[2:9], v[216:223], v[130:133], v188, v189 op_sel_hi:[0,0,0]
	v_mfma_scale_f32_16x16x128_f8f6f4 v[118:121], v[10:17], v[224:231], v[118:121], v188, v189 op_sel_hi:[0,0,0]
	v_mfma_scale_f32_16x16x128_f8f6f4 v[114:117], v[2:9], v[224:231], v[114:117], v188, v189 op_sel_hi:[0,0,0]
	v_mfma_scale_f32_16x16x128_f8f6f4 v[102:105], v[10:17], v[232:239], v[102:105], v188, v189 op_sel_hi:[0,0,0]
	v_mfma_scale_f32_16x16x128_f8f6f4 v[98:101], v[2:9], v[232:239], v[98:101], v188, v189 op_sel_hi:[0,0,0]
	s_setprio 0
	s_barrier
	s_mov_b32 m0, s61
	v_lshl_add_u64 v[176:177], v[176:177], 0, s[18:19]
	ds_read_b128 v[208:211], v193 offset:49152
	ds_read_b128 v[212:215], v193 offset:50176
	ds_read_b128 v[216:219], v193 offset:51200
	ds_read_b128 v[220:223], v193 offset:52224
	ds_read_b128 v[224:227], v193 offset:53248
	ds_read_b128 v[228:231], v193 offset:54272
	ds_read_b128 v[232:235], v193 offset:55296
	ds_read_b128 v[236:239], v193 offset:56320
	global_load_lds_dwordx4 v[176:177], off
	v_lshl_add_u64 v[176:177], v[178:179], 0, s[18:19]
	s_mov_b32 m0, s62
	s_nop 0
	global_load_lds_dwordx4 v[176:177], off
	v_lshl_add_u64 v[176:177], v[180:181], 0, s[18:19]
	s_mov_b32 m0, s63
	s_nop 0
	global_load_lds_dwordx4 v[176:177], off
	v_lshl_add_u64 v[176:177], v[182:183], 0, s[18:19]
	s_add_i32 m0, s63, 0x2000
	s_nop 0
	global_load_lds_dwordx4 v[176:177], off
	v_lshl_add_u64 v[176:177], v[186:187], 0, s[18:19]
	s_mov_b32 m0, s50
	s_nop 0
	global_load_lds_dwordx4 v[176:177], off
	v_lshl_add_u64 v[176:177], v[184:185], 0, s[18:19]
	s_mov_b32 m0, s51
	s_nop 0
	global_load_lds_dwordx4 v[176:177], off
	s_waitcnt vmcnt(9)
	s_waitcnt lgkmcnt(0)
	s_barrier
	s_setprio 1
	s_waitcnt lgkmcnt(0)
	v_mfma_scale_f32_16x16x128_f8f6f4 v[94:97], v[26:33], v[208:215], v[94:97], v188, v189 op_sel_hi:[0,0,0]
	v_mfma_scale_f32_16x16x128_f8f6f4 v[90:93], v[18:25], v[208:215], v[90:93], v188, v189 op_sel_hi:[0,0,0]
	v_mfma_scale_f32_16x16x128_f8f6f4 v[78:81], v[26:33], v[216:223], v[78:81], v188, v189 op_sel_hi:[0,0,0]
	v_mfma_scale_f32_16x16x128_f8f6f4 v[74:77], v[18:25], v[216:223], v[74:77], v188, v189 op_sel_hi:[0,0,0]
	v_mfma_scale_f32_16x16x128_f8f6f4 v[62:65], v[26:33], v[224:231], v[62:65], v188, v189 op_sel_hi:[0,0,0]
	v_mfma_scale_f32_16x16x128_f8f6f4 v[58:61], v[18:25], v[224:231], v[58:61], v188, v189 op_sel_hi:[0,0,0]
	v_mfma_scale_f32_16x16x128_f8f6f4 v[46:49], v[26:33], v[232:239], v[46:49], v188, v189 op_sel_hi:[0,0,0]
	v_mfma_scale_f32_16x16x128_f8f6f4 v[42:45], v[18:25], v[232:239], v[42:45], v188, v189 op_sel_hi:[0,0,0]
	s_setprio 0
	s_setprio 1
	v_mfma_scale_f32_16x16x128_f8f6f4 v[86:89], v[10:17], v[208:215], v[86:89], v188, v189 op_sel_hi:[0,0,0]
	v_mfma_scale_f32_16x16x128_f8f6f4 v[82:85], v[2:9], v[208:215], v[82:85], v188, v189 op_sel_hi:[0,0,0]
	v_mfma_scale_f32_16x16x128_f8f6f4 v[70:73], v[10:17], v[216:223], v[70:73], v188, v189 op_sel_hi:[0,0,0]
	v_mfma_scale_f32_16x16x128_f8f6f4 v[66:69], v[2:9], v[216:223], v[66:69], v188, v189 op_sel_hi:[0,0,0]
	v_mfma_scale_f32_16x16x128_f8f6f4 v[54:57], v[10:17], v[224:231], v[54:57], v188, v189 op_sel_hi:[0,0,0]
	v_mfma_scale_f32_16x16x128_f8f6f4 v[50:53], v[2:9], v[224:231], v[50:53], v188, v189 op_sel_hi:[0,0,0]
	v_mfma_scale_f32_16x16x128_f8f6f4 v[38:41], v[10:17], v[232:239], v[38:41], v188, v189 op_sel_hi:[0,0,0]
	v_mfma_scale_f32_16x16x128_f8f6f4 v[34:37], v[2:9], v[232:239], v[34:37], v188, v189 op_sel_hi:[0,0,0]
	s_setprio 0
	s_barrier
	s_add_u32 s34, s34, 0x100
	s_addc_u32 s35, s35, 0
	s_add_u32 s36, s36, 0x100
	s_addc_u32 s37, s37, 0
	s_cmp_ge_i32 s23, s49
	s_cbranch_scc1 .LBB0_1444
	s_branch .LBB0_1443
